# adds: s5c block-Toeplitz loops with scalar lag tests, all fragment reads of an iteration in flight
# speedup vs baseline: 1.0326x; 1.0024x over previous
; __device__ __forceinline__ void phase_s5c(const Params& P, unsigned char* smraw, int bid, int nb) {
;     ...
;         for (int dir = 0; dir < 2; ++dir) {
;             const int dg = dir * 32 + g;
;             __syncthreads();
;             for (int e = tid; e < 4096; e += NTHR) *(u32x4*)&Fs[(size_t)e * 8] = *(const u32x4*)(S5F + (size_t)dg * 32768 + (size_t)e * 8);
;             __syncthreads();
; #pragma unroll 2
;             for (int i = 0; i < 64; ++i) {
;                 const bf16x8 b = *(const bf16x8*)&Us[(i * 64 + lane) * 8];
; #pragma unroll
;                 for (int m = 0; m < 4; ++m) {
;                     const int mt = wave + 8 * m;
;                     const int d = dir == 0 ? 2 * mt - i + 1 : i - 2 * mt;
;                     if (d >= 0 && d < 64) {
;                         const bf16x8 a = *(const bf16x8*)&Fs[(d * 64 + lane) * 8];
;                         acc[m] = __builtin_amdgcn_mfma_f32_32x32x16_bf16(a, b, acc[m], 0, 0, 0);
;                     }
;                 }
;             }
.LBB0_1957:
	s_or_b64 exec, exec, s[0:1]
	v_mov_b32_e32 v50, v79
	v_mov_b32_e32 v51, v79
	v_mov_b32_e32 v52, v79
	v_mov_b32_e32 v53, v79
	v_mov_b32_e32 v54, v79
	v_mov_b32_e32 v55, v79
	v_mov_b32_e32 v56, v79
	v_mov_b32_e32 v57, v79
	v_mov_b32_e32 v58, v79
	v_mov_b32_e32 v59, v79
	v_mov_b32_e32 v60, v79
	v_mov_b32_e32 v61, v79
	v_mov_b32_e32 v62, v79
	v_mov_b32_e32 v63, v79
	v_mov_b32_e32 v64, v79
	v_mov_b32_e32 v65, v79
	v_mov_b64_e32 v[34:35], v[50:51]
	v_mov_b64_e32 v[18:19], v[50:51]
	v_mov_b64_e32 v[2:3], v[50:51]
	s_add_i32 s52, 0, 16
	s_mov_b32 s53, 0
	v_mov_b32_e32 v70, v84
	v_mov_b64_e32 v[36:37], v[52:53]
	v_mov_b64_e32 v[38:39], v[54:55]
	v_mov_b64_e32 v[40:41], v[56:57]
	v_mov_b64_e32 v[42:43], v[58:59]
	v_mov_b64_e32 v[44:45], v[60:61]
	v_mov_b64_e32 v[46:47], v[62:63]
	v_mov_b64_e32 v[48:49], v[64:65]
	v_mov_b64_e32 v[20:21], v[52:53]
	v_mov_b64_e32 v[22:23], v[54:55]
	v_mov_b64_e32 v[24:25], v[56:57]
	v_mov_b64_e32 v[26:27], v[58:59]
	v_mov_b64_e32 v[28:29], v[60:61]
	v_mov_b64_e32 v[30:31], v[62:63]
	v_mov_b64_e32 v[32:33], v[64:65]
	v_mov_b64_e32 v[4:5], v[52:53]
	v_mov_b64_e32 v[6:7], v[54:55]
	v_mov_b64_e32 v[8:9], v[56:57]
	v_mov_b64_e32 v[10:11], v[58:59]
	v_mov_b64_e32 v[12:13], v[60:61]
	v_mov_b64_e32 v[14:15], v[62:63]
	v_mov_b64_e32 v[16:17], v[64:65]
	s_waitcnt lgkmcnt(0)
	s_barrier
	v_readfirstlane_b32 s100, v81
	s_branch .Ltp_d0_top
.Ltp_d0_top:
	v_add_u32_e32 v71, s52, v114
	ds_read_b128 v[66:69], v71
	ds_read_b128 v[152:155], v71 offset:1024
	s_add_i32 s98, s53, s100
	s_add_i32 s99, s98, 0
	s_cmp_lt_u32 s99, 64
	s_cbranch_scc0 .Ltp_d0_r0
	v_add3_u32 v73, v70, v114, s24
	ds_read_b128 v[124:127], v73 offset:1024
.Ltp_d0_r0:
	s_add_i32 s99, s98, 0
	s_cmp_lt_u32 s99, 64
	s_cbranch_scc0 .Ltp_d0_r1
	v_add3_u32 v73, v70, v114, s24
	ds_read_b128 v[128:131], v73
.Ltp_d0_r1:
	s_add_i32 s99, s98, 16
	s_cmp_lt_u32 s99, 64
	s_cbranch_scc0 .Ltp_d0_r2
	v_add3_u32 v73, v70, v114, s35
	ds_read_b128 v[132:135], v73 offset:1024
.Ltp_d0_r2:
	s_add_i32 s99, s98, 16
	s_cmp_lt_u32 s99, 64
	s_cbranch_scc0 .Ltp_d0_r3
	v_add3_u32 v73, v70, v114, s35
	ds_read_b128 v[136:139], v73
.Ltp_d0_r3:
	s_add_i32 s99, s98, 32
	s_cmp_lt_u32 s99, 64
	s_cbranch_scc0 .Ltp_d0_r4
	v_add3_u32 v73, v70, v114, s36
	ds_read_b128 v[140:143], v73 offset:1024
.Ltp_d0_r4:
	s_add_i32 s99, s98, 32
	s_cmp_lt_u32 s99, 64
	s_cbranch_scc0 .Ltp_d0_r5
	v_add3_u32 v73, v70, v114, s36
	ds_read_b128 v[144:147], v73
.Ltp_d0_r5:
	s_add_i32 s99, s98, 48
	s_cmp_lt_u32 s99, 64
	s_cbranch_scc0 .Ltp_d0_r6
	v_add3_u32 v73, v70, v114, s37
	ds_read_b128 v[148:151], v73 offset:1024
.Ltp_d0_r6:
	s_waitcnt lgkmcnt(0)
	s_add_i32 s99, s98, 0
	s_cmp_lt_u32 s99, 64
	s_cbranch_scc0 .Ltp_d0_a0
	v_mfma_f32_32x32x16_bf16 v[50:65], v[124:127], v[66:69], v[50:65]
.Ltp_d0_a0:
	s_add_i32 s99, s98, 48
	s_cmp_lt_u32 s99, 64
	s_cbranch_scc0 .Ltp_d0_r7
	v_add3_u32 v73, v70, v114, s37
	ds_read_b128 v[124:127], v73
.Ltp_d0_r7:
	s_add_i32 s99, s98, 16
	s_cmp_lt_u32 s99, 64
	s_cbranch_scc0 .Ltp_d0_a1
	v_mfma_f32_32x32x16_bf16 v[34:49], v[132:135], v[66:69], v[34:49]
.Ltp_d0_a1:
	s_add_i32 s99, s98, 32
	s_cmp_lt_u32 s99, 64
	s_cbranch_scc0 .Ltp_d0_a2
	v_mfma_f32_32x32x16_bf16 v[18:33], v[140:143], v[66:69], v[18:33]
.Ltp_d0_a2:
	s_add_i32 s99, s98, 48
	s_cmp_lt_u32 s99, 64
	s_cbranch_scc0 .Ltp_d0_a3
	v_mfma_f32_32x32x16_bf16 v[2:17], v[148:151], v[66:69], v[2:17]
.Ltp_d0_a3:
	s_add_i32 s99, s98, 0
	s_cmp_lt_u32 s99, 64
	s_cbranch_scc0 .Ltp_d0_b0
	v_mfma_f32_32x32x16_bf16 v[50:65], v[128:131], v[152:155], v[50:65]
.Ltp_d0_b0:
	s_add_i32 s99, s98, 16
	s_cmp_lt_u32 s99, 64
	s_cbranch_scc0 .Ltp_d0_b1
	v_mfma_f32_32x32x16_bf16 v[34:49], v[136:139], v[152:155], v[34:49]
.Ltp_d0_b1:
	s_add_i32 s99, s98, 32
	s_cmp_lt_u32 s99, 64
	s_cbranch_scc0 .Ltp_d0_b2
	v_mfma_f32_32x32x16_bf16 v[18:33], v[144:147], v[152:155], v[18:33]
.Ltp_d0_b2:
	s_add_i32 s99, s98, 48
	s_cmp_lt_u32 s99, 64
	s_cbranch_scc0 .Ltp_d0_b3
	s_waitcnt lgkmcnt(0)
	v_mfma_f32_32x32x16_bf16 v[2:17], v[124:127], v[152:155], v[2:17]
.Ltp_d0_b3:
	s_addk_i32 s52, 0x800
	s_add_i32 s53, s53, -2
	v_add_u32_e32 v70, 0xfffff800, v70
	s_cmpk_eq_i32 s53, 0xffc0
	s_cbranch_scc0 .Ltp_d0_top
	s_branch .LBB0_1975

; __device__ __forceinline__ void phase_s5c(const Params& P, unsigned char* smraw, int bid, int nb) {
;     ...
;         for (int dir = 0; dir < 2; ++dir) {
;             const int dg = dir * 32 + g;
;             __syncthreads();
;             for (int e = tid; e < 4096; e += NTHR) *(u32x4*)&Fs[(size_t)e * 8] = *(const u32x4*)(S5F + (size_t)dg * 32768 + (size_t)e * 8);
;             __syncthreads();
; #pragma unroll 2
;             for (int i = 0; i < 64; ++i) {
;                 const bf16x8 b = *(const bf16x8*)&Us[(i * 64 + lane) * 8];
; #pragma unroll
;                 for (int m = 0; m < 4; ++m) {
;                     const int mt = wave + 8 * m;
;                     const int d = dir == 0 ? 2 * mt - i + 1 : i - 2 * mt;
;                     if (d >= 0 && d < 64) {
;                         const bf16x8 a = *(const bf16x8*)&Fs[(d * 64 + lane) * 8];
;                         acc[m] = __builtin_amdgcn_mfma_f32_32x32x16_bf16(a, b, acc[m], 0, 0, 0);
;                     }
;                 }
;             }
.LBB0_1979:
	s_or_b64 exec, exec, s[0:1]
	s_mov_b32 s8, 0
	v_mov_b32_e32 v72, v75
	s_waitcnt lgkmcnt(0)
	s_barrier
	v_readfirstlane_b32 s101, v117
	s_branch .Ltp_d1_top
.Ltp_d1_top:
	ds_read_b128 v[66:69], v72 offset:16
	ds_read_b128 v[152:155], v72 offset:1040
	v_add_u32_e32 v78, v72, v116
	s_add_i32 s98, s8, s101
	s_add_i32 s99, s98, 0
	s_cmp_lt_u32 s99, 64
	s_cbranch_scc0 .Ltp_d1_r0
	v_add3_u32 v73, v72, v116, s24
	ds_read_b128 v[124:127], v73
.Ltp_d1_r0:
	s_add_i32 s99, s98, 1
	s_cmp_lt_u32 s99, 64
	s_cbranch_scc0 .Ltp_d1_r1
	v_add3_u32 v73, v72, v116, s29
	ds_read_b128 v[128:131], v73
.Ltp_d1_r1:
	s_add_i32 s99, s98, -16
	s_cmp_lt_u32 s99, 64
	s_cbranch_scc0 .Ltp_d1_r2
	ds_read_b128 v[132:135], v78 offset:49168
.Ltp_d1_r2:
	s_add_i32 s99, s98, -15
	s_cmp_lt_u32 s99, 64
	s_cbranch_scc0 .Ltp_d1_r3
	ds_read_b128 v[136:139], v78 offset:50192
.Ltp_d1_r3:
	s_add_i32 s99, s98, -32
	s_cmp_lt_u32 s99, 64
	s_cbranch_scc0 .Ltp_d1_r4
	ds_read_b128 v[140:143], v78 offset:32784
.Ltp_d1_r4:
	s_add_i32 s99, s98, -31
	s_cmp_lt_u32 s99, 64
	s_cbranch_scc0 .Ltp_d1_r5
	ds_read_b128 v[144:147], v78 offset:33808
.Ltp_d1_r5:
	s_add_i32 s99, s98, -48
	s_cmp_lt_u32 s99, 64
	s_cbranch_scc0 .Ltp_d1_r6
	ds_read_b128 v[148:151], v78 offset:16400

; __device__ __forceinline__ void phase_s5c(const Params& P, unsigned char* smraw, int bid, int nb) {
;     ...
;         for (int dir = 0; dir < 2; ++dir) {
;             const int dg = dir * 32 + g;
;             __syncthreads();
;             for (int e = tid; e < 4096; e += NTHR) *(u32x4*)&Fs[(size_t)e * 8] = *(const u32x4*)(S5F + (size_t)dg * 32768 + (size_t)e * 8);
;             __syncthreads();
; #pragma unroll 2
;             for (int i = 0; i < 64; ++i) {
;                 const bf16x8 b = *(const bf16x8*)&Us[(i * 64 + lane) * 8];
; #pragma unroll
;                 for (int m = 0; m < 4; ++m) {
;                     const int mt = wave + 8 * m;
;                     const int d = dir == 0 ? 2 * mt - i + 1 : i - 2 * mt;
;                     if (d >= 0 && d < 64) {
;                         const bf16x8 a = *(const bf16x8*)&Fs[(d * 64 + lane) * 8];
;                         acc[m] = __builtin_amdgcn_mfma_f32_32x32x16_bf16(a, b, acc[m], 0, 0, 0);
;                     }
;                 }
;             }
.Ltp_d1_a0:
	s_add_i32 s99, s98, -47
	s_cmp_lt_u32 s99, 64
	s_cbranch_scc0 .Ltp_d1_r7
	ds_read_b128 v[124:127], v78 offset:17424
.Ltp_d1_r7:
	s_add_i32 s99, s98, -16
	s_cmp_lt_u32 s99, 64
	s_cbranch_scc0 .Ltp_d1_a1
	v_mfma_f32_32x32x16_bf16 v[34:49], v[132:135], v[66:69], v[34:49]
.Ltp_d1_a1:
	s_add_i32 s99, s98, -32
	s_cmp_lt_u32 s99, 64
	s_cbranch_scc0 .Ltp_d1_a2
	v_mfma_f32_32x32x16_bf16 v[18:33], v[140:143], v[66:69], v[18:33]
.Ltp_d1_a2:
	s_add_i32 s99, s98, -48
	s_cmp_lt_u32 s99, 64
	s_cbranch_scc0 .Ltp_d1_a3
	v_mfma_f32_32x32x16_bf16 v[2:17], v[148:151], v[66:69], v[2:17]
.Ltp_d1_a3:
	s_add_i32 s99, s98, 1
	s_cmp_lt_u32 s99, 64
	s_cbranch_scc0 .Ltp_d1_b0
	v_mfma_f32_32x32x16_bf16 v[50:65], v[128:131], v[152:155], v[50:65]
.Ltp_d1_b0:
	s_add_i32 s99, s98, -15
	s_cmp_lt_u32 s99, 64
	s_cbranch_scc0 .Ltp_d1_b1
	v_mfma_f32_32x32x16_bf16 v[34:49], v[136:139], v[152:155], v[34:49]
.Ltp_d1_b1:
	s_add_i32 s99, s98, -31
	s_cmp_lt_u32 s99, 64
	s_cbranch_scc0 .Ltp_d1_b2
	v_mfma_f32_32x32x16_bf16 v[18:33], v[144:147], v[152:155], v[18:33]
.Ltp_d1_b2:
	s_add_i32 s99, s98, -47
	s_cmp_lt_u32 s99, 64
	s_cbranch_scc0 .Ltp_d1_b3
	s_waitcnt lgkmcnt(0)
	v_mfma_f32_32x32x16_bf16 v[2:17], v[124:127], v[152:155], v[2:17]
.Ltp_d1_b3:
	s_add_i32 s8, s8, 2
	v_add_u32_e32 v72, 0x800, v72
	s_cmp_lg_u32 s8, 64
	s_cbranch_scc1 .Ltp_d1_top
	s_branch .LBB0_1997
